# v13 + per-iteration L2 prefetch of next codebook slice (for codeword gathers)
# speedup vs baseline: 1.0715x; 1.0715x over previous
.LBB2_414:
	s_movk_i32 s0, 0xc00
	v_mov_b64_e32 v[26:27], s[42:43]
	v_mul_u32_u24_e32 v28, 0xc00, v154
	v_mad_i64_i32 v[26:27], s[0:1], v62, s0, v[26:27]
	v_or_b32_e32 v28, v28, v98
	v_mov_b32_e32 v99, 0
	v_lshl_add_u64 v[26:27], v[26:27], 0, v[98:99]
	v_or_b32_e32 v29, 0x10000, v28
	global_store_dwordx4 v[26:27], v[22:25], off sc1
	ds_write_b128 v29, v[22:25]
	v_sub_f32_e32 v10, v10, v22
	v_or_b32_e32 v22, v101, v154
	v_sub_f32_e32 v11, v11, v23
	v_add_u32_e32 v23, v22, v102
	v_lshl_or_b32 v23, v23, 4, v103
	ds_write_b32 v23, v10
	v_add_u32_e32 v10, v22, v104
	v_lshl_or_b32 v10, v10, 4, v105
	ds_write_b32 v10, v11
	v_or_b32_e32 v10, v106, v154
	v_add_u32_e32 v10, v10, v107
	v_sub_f32_e32 v12, v12, v24
	v_lshl_or_b32 v10, v10, 4, v108
	ds_write_b32 v10, v12
	v_or_b32_e32 v10, v109, v154
	v_add_u32_e32 v10, v10, v110
	v_sub_f32_e32 v13, v13, v25
	v_lshl_or_b32 v10, v10, 4, v111
	ds_write_b32 v10, v13
	v_add_u32_e32 v10, 0x10400, v28
	ds_write_b128 v10, v[18:21]
	v_sub_f32_e32 v10, v6, v18
	v_sub_f32_e32 v11, v7, v19
	v_pk_add_f32 v[6:7], v[8:9], v[20:21] neg_lo:[0,1] neg_hi:[0,1]
	v_or_b32_e32 v8, v112, v154
	v_add_u32_e32 v9, v8, v113
	v_add_u32_e32 v8, v8, v115
	v_lshl_or_b32 v9, v9, 4, v114
	v_lshl_or_b32 v8, v8, 4, v116
	ds_write_b32 v9, v10
	ds_write_b32 v8, v11
	v_or_b32_e32 v8, v117, v154
	v_add_u32_e32 v8, v8, v118
	v_lshl_or_b32 v8, v8, 4, v119
	ds_write_b32 v8, v6
	v_or_b32_e32 v6, v120, v154
	v_add_u32_e32 v6, v6, v121
	v_lshl_or_b32 v6, v6, 4, v122
	ds_write_b32 v6, v7
	v_add_u32_e32 v6, 0x10800, v28
	ds_write_b128 v6, v[14:17]
	v_or_b32_e32 v6, v123, v154
	v_add_u32_e32 v7, v6, v124
	v_pk_add_f32 v[2:3], v[2:3], v[14:15] neg_lo:[0,1] neg_hi:[0,1]
	v_lshl_or_b32 v7, v7, 4, v125
	ds_write_b32 v7, v2
	v_add_u32_e32 v2, v6, v126
	v_lshl_or_b32 v2, v2, 4, v127
	ds_write_b32 v2, v3
	v_or_b32_e32 v2, v133, v154
	v_add_u32_e32 v2, v2, v134
	v_pk_add_f32 v[4:5], v[4:5], v[16:17] neg_lo:[0,1] neg_hi:[0,1]
	v_lshl_or_b32 v2, v2, 4, v63
	ds_write_b32 v2, v4
	v_or_b32_e32 v2, v135, v154
	v_add_u32_e32 v2, v2, v132
	v_lshl_or_b32 v2, v2, 4, v136
	v_add_lshl_u32 v4, v100, v154, 4
	s_mov_b32 s5, 0
	s_mov_b32 s4, 1.0
	ds_write_b32 v2, v5
	v_mov_b64_e32 v[2:3], s[4:5]
	v_add_u32_e32 v4, 8, v4
	s_waitcnt vmcnt(1)
	v_lshlrev_b32_e32 v40, 9, v150
	ds_write2st64_b64 v4, v[2:3], v[2:3] offset1:64
	v_or_b32_e32 v2, v40, v128
	v_lshlrev_b32_e32 v98, 4, v2
	v_lshl_add_u64 v[100:101], s[40:41], 0, v[98:99]
	s_mov_b64 s[0:1], 0x787000
	v_lshl_add_u64 v[34:35], v[100:101], 0, s[0:1]
	s_mov_b32 s0, 0x788000
	v_add_co_u32_e32 v36, vcc, s0, v100
	global_store_dwordx4 v[26:27], v[18:21], off offset:1024 sc1
	global_store_dwordx4 v[26:27], v[14:17], off offset:2048 sc1
	s_lshr_b32 s59, s33, 4
	s_and_b32 s59, s59, 31
	s_lshl_b32 s59, s59, 15
	s_add_u32 s59, s59, 0x787000
	s_add_u32 s68, s40, s59
	s_addc_u32 s69, s41, 0
	v_lshlrev_b32_e32 v207, 6, v0
	global_load_dword v207, v207, s[68:69]
	s_waitcnt lgkmcnt(0)
	s_barrier
	v_addc_co_u32_e32 v37, vcc, 0, v101, vcc
	global_load_dwordx4 v[2:5], v[34:35], off offset:1024
	global_load_dwordx4 v[10:13], v[34:35], off offset:2048
	global_load_dwordx4 v[14:17], v[34:35], off offset:3072
	global_load_dwordx4 v[6:9], v[36:37], off offset:-4096
	global_load_dwordx4 v[18:21], v[36:37], off
	global_load_dwordx4 v[22:25], v[36:37], off offset:1024
	global_load_dwordx4 v[26:29], v[36:37], off offset:2048
	global_load_dwordx4 v[30:33], v[36:37], off offset:3072
	v_and_b32_e32 v35, 15, v0
	v_lshrrev_b32_e32 v37, 4, v128
	v_lshlrev_b32_e32 v102, 2, v35
	v_lshlrev_b32_e32 v41, 2, v37
	v_lshlrev_b32_e32 v34, 4, v35
	v_cmp_gt_u32_e64 s[0:1], 6, v35
	v_mov_b32_e32 v35, v99
	v_or3_b32 v36, v34, v41, v40
	v_lshl_add_u64 v[104:105], s[44:45], 0, v[34:35]
	v_or_b32_e32 v34, v40, v34
	s_movk_i32 s4, 0x1000
	v_or3_b32 v153, v34, v41, s4
	v_or_b32_e32 v34, 0x11800, v98
	v_lshl_add_u64 v[118:119], s[40:41], 0, v[34:35]
	v_or_b32_e32 v34, 0x11400, v98
	v_lshl_add_u64 v[120:121], s[40:41], 0, v[34:35]
	v_or_b32_e32 v34, 0x11000, v98
	ds_read2st64_b32 v[132:133], v36 offset1:1
	v_or_b32_e32 v36, s33, v41
	v_lshl_add_u64 v[122:123], s[40:41], 0, v[34:35]
	v_or_b32_e32 v34, 0x10c00, v98
	v_or_b32_e32 v38, 1, v36
	v_lshl_add_u64 v[124:125], s[40:41], 0, v[34:35]
	v_or_b32_e32 v34, 0x10800, v98
	v_mul_u32_u24_e32 v152, 0x3000, v37
	v_ashrrev_i32_e32 v37, 31, v36
	v_ashrrev_i32_e32 v39, 31, v38
	v_lshl_add_u64 v[126:127], s[40:41], 0, v[34:35]
	v_or_b32_e32 v34, 0x10400, v98
	v_mov_b32_e32 v103, v99
	v_lshlrev_b64 v[108:109], 17, v[36:37]
	v_lshlrev_b64 v[110:111], 17, v[38:39]
	v_or_b32_e32 v38, 2, v36
	v_or_b32_e32 v36, 3, v36
	v_lshl_add_u64 v[128:129], s[40:41], 0, v[34:35]
	v_mul_u32_u24_e32 v34, 24, v150
	v_lshl_add_u64 v[106:107], s[38:39], 0, v[102:103]
	v_ashrrev_i32_e32 v39, 31, v38
	v_ashrrev_i32_e32 v37, 31, v36
	v_lshlrev_b32_e32 v103, 2, v0
	v_or_b32_e32 v98, 0x11c00, v98
	v_or_b32_e32 v34, v152, v34
	v_lshlrev_b64 v[112:113], 17, v[38:39]
	v_lshlrev_b64 v[114:115], 17, v[36:37]
	v_and_b32_e32 v116, 0x700, v103
	v_mov_b32_e32 v117, v99
	v_lshl_add_u64 v[130:131], s[40:41], 0, v[98:99]
	v_add_u32_e32 v154, v34, v102
	s_mov_b64 s[6:7], 0
	s_mov_b64 s[8:9], 0x800
	v_mov_b32_e32 v155, 0x400
	v_mov_b32_e32 v159, 0
	v_mov_b32_e32 v158, 0
	v_mov_b32_e32 v157, 0
	v_mov_b32_e32 v156, 0
	v_readfirstlane_b32 s78, v150
	v_and_b32_e32 v104, 63, v0
	v_lshlrev_b32_e32 v104, 4, v104
	v_lshl_or_b32 v104, v150, 13, v104
	v_add_u32_e32 v105, 0xfffff000, v153
	v_mov_b32_e32 v106, v154
	v_lshrrev_b32_e32 v98, 2, v102
	v_cmp_gt_u32_e32 vcc, 6, v98
	v_add_u32_e32 v107, -6, v98
	s_nop 0
	v_cndmask_b32_e32 v107, v107, v98, vcc
	v_cmp_gt_u32_e32 vcc, 6, v107
	v_add_u32_e32 v98, -6, v107
	s_nop 0
	v_cndmask_b32_e32 v107, v98, v107, vcc
	v_lshlrev_b32_e32 v107, 2, v107
	v_sub_u32_e32 v106, v106, v102
	v_add_u32_e32 v106, v106, v107
	v_and_b32_e32 v98, 63, v0
	v_lshrrev_b32_e32 v98, 4, v98
	v_lshlrev_b32_e32 v98, 19, v98
	v_lshl_or_b32 v108, v102, 2, v98
	v_add_u32_e32 v109, 0x20000, v108
	v_add_u32_e32 v110, 0x40000, v108
	v_add_u32_e32 v111, 0x60000, v108
	v_mov_b32_e32 v240, 0
	v_mov_b32_e32 v241, 0
	v_mov_b32_e32 v242, 0
	v_mov_b32_e32 v243, 0
	s_lshl_b32 s84, s33, 17
	s_lshl_b32 s85, s78, 10
	s_add_u32 s84, s84, s85
	s_add_u32 s80, s44, s84
	s_addc_u32 s81, s45, 0
	s_mul_i32 s84, s78, 0x1800
	s_add_u32 s94, s38, s84
	s_addc_u32 s95, s39, 0
	s_mov_b32 s70, 0
	v_and_b32_e32 v100, 63, v0
	v_mul_u32_u24_e32 v100, 0x60, v100
	s_add_u32 s86, s40, 0x797000
	s_addc_u32 s87, s41, 0
	s_add_u32 s88, s86, 0x1000
	s_addc_u32 s89, s87, 0
	v_add_u32_e32 v112, 0x1000, v105
	s_waitcnt vmcnt(0) lgkmcnt(0)
	v_mfma_f32_16x16x4_f32 v[34:37], v132, v6, 0
	v_mfma_f32_16x16x4_f32 v[38:41], v132, v8, 0
	v_mfma_f32_16x16x4_f32 v[34:37], v133, v7, v[34:37]
	v_mfma_f32_16x16x4_f32 v[38:41], v133, v9, v[38:41]
	global_load_dwordx4 v[6:9], v104, s[86:87]
	v_mfma_f32_16x16x4_f32 v[42:45], v132, v2, 0
	v_mfma_f32_16x16x4_f32 v[46:49], v132, v4, 0
	v_mfma_f32_16x16x4_f32 v[42:45], v133, v3, v[42:45]
	v_mfma_f32_16x16x4_f32 v[46:49], v133, v5, v[46:49]
	global_load_dwordx4 v[2:5], v104, s[86:87] offset:1024
	v_mfma_f32_16x16x4_f32 v[50:53], v132, v10, 0
	v_mfma_f32_16x16x4_f32 v[54:57], v132, v12, 0
	v_mfma_f32_16x16x4_f32 v[50:53], v133, v11, v[50:53]
	v_mfma_f32_16x16x4_f32 v[54:57], v133, v13, v[54:57]
	global_load_dwordx4 v[10:13], v104, s[86:87] offset:2048
	v_mfma_f32_16x16x4_f32 v[58:61], v132, v14, 0
	v_mfma_f32_16x16x4_f32 v[62:65], v132, v16, 0
	v_mfma_f32_16x16x4_f32 v[58:61], v133, v15, v[58:61]
	v_mfma_f32_16x16x4_f32 v[62:65], v133, v17, v[62:65]
	global_load_dwordx4 v[14:17], v104, s[86:87] offset:3072
	v_mfma_f32_16x16x4_f32 v[66:69], v132, v18, 0
	v_mfma_f32_16x16x4_f32 v[70:73], v132, v20, 0
	v_mfma_f32_16x16x4_f32 v[66:69], v133, v19, v[66:69]
	v_mfma_f32_16x16x4_f32 v[70:73], v133, v21, v[70:73]
	global_load_dwordx4 v[18:21], v104, s[88:89]
	v_mfma_f32_16x16x4_f32 v[74:77], v132, v22, 0
	v_mfma_f32_16x16x4_f32 v[78:81], v132, v24, 0
	v_mfma_f32_16x16x4_f32 v[74:77], v133, v23, v[74:77]
	v_mfma_f32_16x16x4_f32 v[78:81], v133, v25, v[78:81]
	global_load_dwordx4 v[22:25], v104, s[88:89] offset:1024
	v_mfma_f32_16x16x4_f32 v[82:85], v132, v26, 0
	v_mfma_f32_16x16x4_f32 v[86:89], v132, v28, 0
	v_mfma_f32_16x16x4_f32 v[82:85], v133, v27, v[82:85]
	v_mfma_f32_16x16x4_f32 v[86:89], v133, v29, v[86:89]
	global_load_dwordx4 v[26:29], v104, s[88:89] offset:2048
	v_mfma_f32_16x16x4_f32 v[90:93], v132, v30, 0
	v_mfma_f32_16x16x4_f32 v[94:97], v132, v32, 0
	v_mfma_f32_16x16x4_f32 v[90:93], v133, v31, v[90:93]
	v_mfma_f32_16x16x4_f32 v[94:97], v133, v33, v[94:97]
	global_load_dwordx4 v[30:33], v104, s[88:89] offset:3072
	ds_read2st64_b32 v[132:133], v112 offset1:1
	s_nop 7
	s_nop 7
	v_max3_f32 v114, v34, v38, v42
	v_max3_f32 v116, v46, v50, v54
	v_max3_f32 v114, v114, v58, v62
	v_max3_f32 v116, v116, v66, v70
	v_max3_f32 v114, v114, v74, v78
	v_max3_f32 v116, v116, v82, v86
	v_max3_f32 v114, v114, v90, v94
	v_max_f32_e32 v114, v114, v116
	s_nop 1
	v_max_f32_dpp v114, v114, v114 row_ror:1 row_mask:0xf bank_mask:0xf
	s_nop 1
	v_max_f32_dpp v114, v114, v114 row_ror:2 row_mask:0xf bank_mask:0xf
	s_nop 1
	v_max_f32_dpp v114, v114, v114 row_ror:4 row_mask:0xf bank_mask:0xf
	s_nop 1
	v_max_f32_dpp v114, v114, v114 row_ror:8 row_mask:0xf bank_mask:0xf
	s_waitcnt vmcnt(0) lgkmcnt(0)
.Lk3m_loop:
	s_waitcnt lgkmcnt(0)
	s_lshl_b32 s84, s70, 13
	s_add_u32 s90, s80, s84
	s_addc_u32 s91, s81, 0
	s_mul_i32 s84, s70, 0xc000
	s_add_u32 s92, s94, s84
	s_addc_u32 s93, s95, 0
	s_add_i32 s84, s70, 2
	s_and_b32 s84, s84, 15
	s_lshl_b32 s82, s84, 12
	s_lshl_b32 s84, s84, 16
	s_add_u32 s84, s84, 0x787000
	s_add_u32 s86, s40, s84
	s_addc_u32 s87, s41, 0
	s_add_u32 s88, s86, 0x1000
	s_addc_u32 s89, s87, 0
	s_add_i32 s84, s70, 15
	s_and_b32 s84, s84, 15
	s_mul_i32 s84, s84, 0xc0
	s_add_u32 s83, s84, 0x10000
	v_add_u32_e32 v112, s82, v105
	s_add_i32 s84, s70, 1
	s_and_b32 s84, s84, 15
	s_mul_i32 s84, s84, 0xc000
	s_add_u32 s58, s94, s84
	s_addc_u32 s59, s95, 0
	global_load_dword v98, v100, s[58:59]
	v_sub_f32_e32 v120, v94, v114
	v_cmp_eq_f32_e64 s[72:73], v94, v114
	s_waitcnt vmcnt(28)
	v_mfma_f32_16x16x4_f32 v[176:179], v132, v6, 0
	ds_read2st64_b32 v[254:255], v112 offset1:1
	v_sub_f32_e32 v121, v90, v114
	v_cmp_eq_f32_e64 s[74:75], v90, v114
	v_exp_f32_e32 v149, v120
	v_cndmask_b32_e64 v118, v155, 15, s[72:73]
	v_max3_f32 v115, v35, v39, v43
	v_sub_f32_e32 v120, v86, v114
	v_cmp_eq_f32_e64 s[76:77], v86, v114
	v_exp_f32_e32 v148, v121
	v_cndmask_b32_e64 v118, v118, 14, s[74:75]
	v_mfma_f32_16x16x4_f32 v[180:183], v132, v8, 0
	v_sub_f32_e32 v121, v82, v114
	v_max3_f32 v117, v47, v51, v55
	v_cmp_eq_f32_e64 s[72:73], v82, v114
	v_exp_f32_e32 v147, v120
	v_cndmask_b32_e64 v118, v118, 13, s[76:77]
	v_sub_f32_e32 v120, v78, v114
	v_cmp_eq_f32_e64 s[74:75], v78, v114
	v_max3_f32 v115, v115, v59, v63
	v_exp_f32_e32 v146, v121
	v_cndmask_b32_e64 v118, v118, 12, s[72:73]
	v_mfma_f32_16x16x4_f32 v[176:179], v133, v7, v[176:179]
	v_sub_f32_e32 v121, v74, v114
	v_cmp_eq_f32_e64 s[76:77], v74, v114
	v_exp_f32_e32 v145, v120
	v_cndmask_b32_e64 v118, v118, 11, s[74:75]
	v_max3_f32 v117, v117, v67, v71
	v_sub_f32_e32 v120, v70, v114
	v_cmp_eq_f32_e64 s[72:73], v70, v114
	v_exp_f32_e32 v144, v121
	v_cndmask_b32_e64 v118, v118, 10, s[76:77]
	v_mfma_f32_16x16x4_f32 v[180:183], v133, v9, v[180:183]
	global_load_dwordx4 v[6:9], v104, s[86:87]
	v_sub_f32_e32 v121, v66, v114
	v_max3_f32 v115, v115, v75, v79
	v_cmp_eq_f32_e64 s[74:75], v66, v114
	v_exp_f32_e32 v143, v120
	v_cndmask_b32_e64 v118, v118, 9, s[72:73]
	v_sub_f32_e32 v120, v62, v114
	v_cmp_eq_f32_e64 s[76:77], v62, v114
	v_max3_f32 v117, v117, v83, v87
	v_exp_f32_e32 v142, v121
	v_cndmask_b32_e64 v118, v118, 8, s[74:75]
	s_waitcnt vmcnt(28)
	v_mfma_f32_16x16x4_f32 v[184:187], v132, v2, 0
	v_sub_f32_e32 v121, v58, v114
	v_cmp_eq_f32_e64 s[72:73], v58, v114
	v_exp_f32_e32 v141, v120
	v_cndmask_b32_e64 v118, v118, 7, s[76:77]
	v_max3_f32 v115, v115, v91, v95
	v_sub_f32_e32 v120, v54, v114
	v_cmp_eq_f32_e64 s[74:75], v54, v114
	v_exp_f32_e32 v140, v121
	v_cndmask_b32_e64 v118, v118, 6, s[72:73]
	v_mfma_f32_16x16x4_f32 v[188:191], v132, v4, 0
	v_sub_f32_e32 v121, v50, v114
	v_max_f32_e32 v115, v115, v117
	v_cmp_eq_f32_e64 s[76:77], v50, v114
	v_exp_f32_e32 v139, v120
	v_cndmask_b32_e64 v118, v118, 5, s[74:75]
	v_sub_f32_e32 v120, v46, v114
	v_cmp_eq_f32_e64 s[72:73], v46, v114
	v_max_f32_dpp v115, v115, v115 row_ror:1 row_mask:0xf bank_mask:0xf
	v_exp_f32_e32 v138, v121
	v_cndmask_b32_e64 v118, v118, 4, s[76:77]
	v_mfma_f32_16x16x4_f32 v[184:187], v133, v3, v[184:187]
	v_sub_f32_e32 v121, v42, v114
	v_cmp_eq_f32_e64 s[74:75], v42, v114
	v_exp_f32_e32 v137, v120
	v_cndmask_b32_e64 v118, v118, 3, s[72:73]
	v_max_f32_dpp v115, v115, v115 row_ror:2 row_mask:0xf bank_mask:0xf
	v_sub_f32_e32 v120, v38, v114
	v_cmp_eq_f32_e64 s[76:77], v38, v114
	v_exp_f32_e32 v136, v121
	v_cndmask_b32_e64 v118, v118, 2, s[74:75]
	v_mfma_f32_16x16x4_f32 v[188:191], v133, v5, v[188:191]
	global_load_dwordx4 v[2:5], v104, s[86:87] offset:1024
	v_sub_f32_e32 v121, v34, v114
	v_max_f32_dpp v115, v115, v115 row_ror:4 row_mask:0xf bank_mask:0xf
	v_cmp_eq_f32_e64 s[72:73], v34, v114
	v_exp_f32_e32 v135, v120
	v_cndmask_b32_e64 v118, v118, 1, s[76:77]
	v_exp_f32_e32 v134, v121
	v_cndmask_b32_e64 v118, v118, 0, s[72:73]
	v_max_f32_dpp v115, v115, v115 row_ror:8 row_mask:0xf bank_mask:0xf
	v_sub_f32_e32 v120, v95, v115
	v_cmp_eq_f32_e64 s[72:73], v95, v115
	v_max3_f32 v114, v36, v40, v44
	s_waitcnt vmcnt(28)
	v_mfma_f32_16x16x4_f32 v[192:195], v132, v10, 0
	v_sub_f32_e32 v121, v91, v115
	v_and_b32_e32 v122, 12, v118
	v_cmp_eq_f32_e64 s[74:75], v91, v115
	v_and_b32_e32 v124, 3, v118
	v_exp_f32_e32 v175, v120
	v_add_f32_e32 v128, v134, v135
	v_cndmask_b32_e64 v119, v155, 15, s[72:73]
	v_add_f32_e32 v130, v136, v137
	v_sub_f32_e32 v120, v87, v115
	v_max3_f32 v116, v48, v52, v56
	v_cmp_eq_f32_e64 s[76:77], v87, v115
	v_exp_f32_e32 v174, v121
	v_lshl_or_b32 v122, v122, 4, v124
	v_cndmask_b32_e64 v119, v119, 14, s[74:75]
	v_add_f32_e32 v128, v128, v138
	v_mfma_f32_16x16x4_f32 v[196:199], v132, v12, 0
	v_sub_f32_e32 v121, v83, v115
	v_add_f32_e32 v130, v130, v139
	v_cmp_eq_f32_e64 s[72:73], v83, v115
	v_or_b32_e32 v122, v122, v102
	v_exp_f32_e32 v173, v120
	v_max3_f32 v114, v114, v60, v64
	v_cndmask_b32_e64 v119, v119, 13, s[76:77]
	v_add_f32_e32 v128, v128, v140
	v_sub_f32_e32 v120, v79, v115
	v_cmp_eq_f32_e64 s[74:75], v79, v115
	v_add_f32_e32 v130, v130, v141
	v_exp_f32_e32 v172, v121
	v_max_u32_e32 v126, v122, v118
	v_cndmask_b32_e64 v119, v119, 12, s[72:73]
	v_max3_f32 v116, v116, v68, v72
	v_mfma_f32_16x16x4_f32 v[192:195], v133, v11, v[192:195]
	v_sub_f32_e32 v121, v75, v115
	v_add_f32_e32 v128, v128, v142
	v_cmp_eq_f32_e64 s[76:77], v75, v115
	v_add_f32_e32 v130, v130, v143
	v_exp_f32_e32 v171, v120
	v_min_u32_dpp v126, v126, v126 row_ror:1 row_mask:0xf bank_mask:0xf
	v_cndmask_b32_e64 v119, v119, 11, s[74:75]
	v_sub_f32_e32 v120, v71, v115
	v_add_f32_e32 v128, v128, v144
	v_cmp_eq_f32_e64 s[72:73], v71, v115
	v_max3_f32 v114, v114, v76, v80
	v_exp_f32_e32 v170, v121
	v_add_f32_e32 v130, v130, v145
	v_cndmask_b32_e64 v119, v119, 10, s[76:77]
	v_min_u32_dpp v126, v126, v126 row_ror:2 row_mask:0xf bank_mask:0xf
	v_mfma_f32_16x16x4_f32 v[196:199], v133, v13, v[196:199]
	global_load_dwordx4 v[10:13], v104, s[86:87] offset:2048
	v_sub_f32_e32 v121, v67, v115
	v_add_f32_e32 v128, v128, v146
	v_cmp_eq_f32_e64 s[74:75], v67, v115
	v_max3_f32 v116, v116, v84, v88
	v_exp_f32_e32 v169, v120
	v_cndmask_b32_e64 v119, v119, 9, s[72:73]
	v_add_f32_e32 v130, v130, v147
	v_sub_f32_e32 v120, v63, v115
	v_min_u32_dpp v126, v126, v126 row_ror:4 row_mask:0xf bank_mask:0xf
	v_cmp_eq_f32_e64 s[76:77], v63, v115
	v_add_f32_e32 v128, v128, v148
	v_exp_f32_e32 v168, v121
	v_add_f32_e32 v130, v130, v149
	v_cndmask_b32_e64 v119, v119, 8, s[74:75]
	v_max3_f32 v114, v114, v92, v96
	s_waitcnt vmcnt(25)
	v_mfma_f32_16x16x4_f32 v[200:203], v132, v14, 0
	v_sub_f32_e32 v121, v59, v115
	v_min_u32_dpp v126, v126, v126 row_ror:8 row_mask:0xf bank_mask:0xf
	v_cmp_eq_f32_e64 s[72:73], v59, v115
	v_exp_f32_e32 v167, v120
	v_add_f32_e32 v128, v128, v130
	v_cndmask_b32_e64 v119, v119, 7, s[76:77]
	v_mad_u32_u24 v248, v126, 24, v107
	v_sub_f32_e32 v120, v55, v115
	v_add_f32_dpp v128, v128, v128 row_ror:1 row_mask:0xf bank_mask:0xf
	v_cmp_eq_f32_e64 s[74:75], v55, v115
	v_max_f32_e32 v114, v114, v116
	v_exp_f32_e32 v166, v121
	global_load_dword v240, v248, s[92:93]
	v_cndmask_b32_e64 v119, v119, 6, s[72:73]
	v_add_f32_dpp v128, v128, v128 row_ror:2 row_mask:0xf bank_mask:0xf
	v_mfma_f32_16x16x4_f32 v[204:207], v132, v16, 0
	v_sub_f32_e32 v121, v51, v115
	v_cmp_eq_f32_e64 s[76:77], v51, v115
	v_add_f32_dpp v128, v128, v128 row_ror:4 row_mask:0xf bank_mask:0xf
	v_exp_f32_e32 v165, v120
	v_max_f32_dpp v114, v114, v114 row_ror:1 row_mask:0xf bank_mask:0xf
	v_cndmask_b32_e64 v119, v119, 5, s[74:75]
	v_add_f32_dpp v128, v128, v128 row_ror:8 row_mask:0xf bank_mask:0xf
	v_sub_f32_e32 v120, v47, v115
	v_rcp_f32_e32 v244, v128
	v_cmp_eq_f32_e64 s[72:73], v47, v115
	v_pk_mul_f32 v[134:135], v[244:245], v[134:135] op_sel_hi:[0,1]
	v_exp_f32_e32 v164, v121
	v_pk_mul_f32 v[136:137], v[244:245], v[136:137] op_sel_hi:[0,1]
	v_cndmask_b32_e64 v119, v119, 4, s[76:77]
	v_mfma_f32_16x16x4_f32 v[200:203], v133, v15, v[200:203]
	v_sub_f32_e32 v121, v43, v115
	v_max_f32_dpp v114, v114, v114 row_ror:2 row_mask:0xf bank_mask:0xf
	v_cmp_eq_f32_e64 s[74:75], v43, v115
	global_store_dwordx4 v108, v[134:137], s[90:91] sc1
	v_exp_f32_e32 v163, v120
	v_pk_mul_f32 v[138:139], v[244:245], v[138:139] op_sel_hi:[0,1]
	v_cndmask_b32_e64 v119, v119, 3, s[72:73]
	v_pk_mul_f32 v[140:141], v[244:245], v[140:141] op_sel_hi:[0,1]
	v_sub_f32_e32 v120, v39, v115
	v_max_f32_dpp v114, v114, v114 row_ror:4 row_mask:0xf bank_mask:0xf
	v_cmp_eq_f32_e64 s[76:77], v39, v115
	global_store_dwordx4 v108, v[138:141], s[90:91] offset:256 sc1
	v_exp_f32_e32 v162, v121
	v_cndmask_b32_e64 v119, v119, 2, s[74:75]
	v_pk_mul_f32 v[142:143], v[244:245], v[142:143] op_sel_hi:[0,1]
	v_mfma_f32_16x16x4_f32 v[204:207], v133, v17, v[204:207]
	global_load_dwordx4 v[14:17], v104, s[86:87] offset:3072
	v_sub_f32_e32 v121, v35, v115
	v_pk_mul_f32 v[144:145], v[244:245], v[144:145] op_sel_hi:[0,1]
	v_cmp_eq_f32_e64 s[72:73], v35, v115
	global_store_dwordx4 v108, v[142:145], s[90:91] offset:512 sc1
	v_exp_f32_e32 v161, v120
	v_max_f32_dpp v114, v114, v114 row_ror:8 row_mask:0xf bank_mask:0xf
	v_cndmask_b32_e64 v119, v119, 1, s[76:77]
	v_pk_mul_f32 v[146:147], v[244:245], v[146:147] op_sel_hi:[0,1]
	v_exp_f32_e32 v160, v121
	v_pk_mul_f32 v[148:149], v[244:245], v[148:149] op_sel_hi:[0,1]
	v_cndmask_b32_e64 v119, v119, 0, s[72:73]
	global_store_dwordx4 v108, v[146:149], s[90:91] offset:768 sc1
	v_sub_f32_e32 v120, v96, v114
	v_cmp_eq_f32_e64 s[72:73], v96, v114
	s_waitcnt vmcnt(14)
	s_waitcnt vmcnt(28)
	v_mfma_f32_16x16x4_f32 v[208:211], v132, v18, 0
	v_sub_f32_e32 v121, v92, v114
	v_add_u32_e32 v113, s83, v106
	v_cmp_eq_f32_e64 s[74:75], v92, v114
	ds_read2st64_b32 v[250:251], v113 offset1:12
	v_exp_f32_e32 v149, v120
	ds_read2st64_b32 v[252:253], v113 offset0:24 offset1:36
	v_cndmask_b32_e64 v118, v155, 15, s[72:73]
	v_max3_f32 v115, v37, v41, v45
	v_sub_f32_e32 v120, v88, v114
	v_and_b32_e32 v123, 12, v119
	v_cmp_eq_f32_e64 s[76:77], v88, v114
	v_and_b32_e32 v125, 3, v119
	v_exp_f32_e32 v148, v121
	v_add_f32_e32 v129, v160, v161
	v_cndmask_b32_e64 v118, v118, 14, s[74:75]
	v_add_f32_e32 v131, v162, v163
	v_mfma_f32_16x16x4_f32 v[212:215], v132, v20, 0
	v_sub_f32_e32 v121, v84, v114
	v_max3_f32 v117, v49, v53, v57
	v_cmp_eq_f32_e64 s[72:73], v84, v114
	v_lshl_or_b32 v123, v123, 4, v125
	v_exp_f32_e32 v147, v120
	v_cndmask_b32_e64 v118, v118, 13, s[76:77]
	v_add_f32_e32 v129, v129, v164
	v_sub_f32_e32 v120, v80, v114
	v_add_f32_e32 v131, v131, v165
	v_cmp_eq_f32_e64 s[74:75], v80, v114
	v_or_b32_e32 v123, v123, v102
	v_exp_f32_e32 v146, v121
	v_max3_f32 v115, v115, v61, v65
	v_cndmask_b32_e64 v118, v118, 12, s[72:73]
	v_add_f32_e32 v129, v129, v166
	v_mfma_f32_16x16x4_f32 v[208:211], v133, v19, v[208:211]
	v_sub_f32_e32 v121, v76, v114
	v_add_f32_e32 v131, v131, v167
	v_cmp_eq_f32_e64 s[76:77], v76, v114
	v_max_u32_e32 v127, v123, v119
	v_exp_f32_e32 v145, v120
	v_max3_f32 v117, v117, v69, v73
	v_cndmask_b32_e64 v118, v118, 11, s[74:75]
	v_add_f32_e32 v129, v129, v168
	v_sub_f32_e32 v120, v72, v114
	v_add_f32_e32 v131, v131, v169
	v_cmp_eq_f32_e64 s[72:73], v72, v114
	v_min_u32_dpp v127, v127, v127 row_ror:1 row_mask:0xf bank_mask:0xf
	v_exp_f32_e32 v144, v121
	v_add_f32_e32 v129, v129, v170
	v_cndmask_b32_e64 v118, v118, 10, s[76:77]
	v_mfma_f32_16x16x4_f32 v[212:215], v133, v21, v[212:215]
	global_load_dwordx4 v[18:21], v104, s[88:89]
	v_sub_f32_e32 v121, v68, v114
	v_max3_f32 v115, v115, v77, v81
	v_cmp_eq_f32_e64 s[74:75], v68, v114
	v_add_f32_e32 v131, v131, v171
	v_exp_f32_e32 v143, v120
	v_min_u32_dpp v127, v127, v127 row_ror:2 row_mask:0xf bank_mask:0xf
	v_cndmask_b32_e64 v118, v118, 9, s[72:73]
	v_add_f32_e32 v129, v129, v172
	v_sub_f32_e32 v120, v64, v114
	v_max3_f32 v117, v117, v85, v89
	v_cmp_eq_f32_e64 s[76:77], v64, v114
	v_add_f32_e32 v131, v131, v173
	v_exp_f32_e32 v142, v121
	v_min_u32_dpp v127, v127, v127 row_ror:4 row_mask:0xf bank_mask:0xf
	v_cndmask_b32_e64 v118, v118, 8, s[74:75]
	v_add_f32_e32 v129, v129, v174
	s_waitcnt vmcnt(25)
	v_mfma_f32_16x16x4_f32 v[216:219], v132, v22, 0
	v_sub_f32_e32 v121, v60, v114
	v_add_f32_e32 v131, v131, v175
	v_cmp_eq_f32_e64 s[72:73], v60, v114
	v_max3_f32 v115, v115, v93, v97
	v_exp_f32_e32 v141, v120
	v_min_u32_dpp v127, v127, v127 row_ror:8 row_mask:0xf bank_mask:0xf
	v_cndmask_b32_e64 v118, v118, 7, s[76:77]
	v_add_f32_e32 v129, v129, v131
	v_sub_f32_e32 v120, v56, v114
	v_cmp_eq_f32_e64 s[74:75], v56, v114
	v_mad_u32_u24 v249, v127, 24, v107
	v_exp_f32_e32 v140, v121
	v_add_f32_dpp v129, v129, v129 row_ror:1 row_mask:0xf bank_mask:0xf
	v_cndmask_b32_e64 v118, v118, 6, s[72:73]
	v_max_f32_e32 v115, v115, v117
	v_mfma_f32_16x16x4_f32 v[220:223], v132, v24, 0
	v_sub_f32_e32 v121, v52, v114
	global_load_dword v241, v249, s[92:93]
	v_cmp_eq_f32_e64 s[76:77], v52, v114
	v_add_f32_dpp v129, v129, v129 row_ror:2 row_mask:0xf bank_mask:0xf
	v_exp_f32_e32 v139, v120
	s_nop 0
	v_add_f32_dpp v129, v129, v129 row_ror:4 row_mask:0xf bank_mask:0xf
	v_cndmask_b32_e64 v118, v118, 5, s[74:75]
	v_max_f32_dpp v115, v115, v115 row_ror:1 row_mask:0xf bank_mask:0xf
	v_sub_f32_e32 v120, v48, v114
	v_add_f32_dpp v129, v129, v129 row_ror:8 row_mask:0xf bank_mask:0xf
	v_cmp_eq_f32_e64 s[72:73], v48, v114
	v_rcp_f32_e32 v246, v129
	v_exp_f32_e32 v138, v121
	v_pk_mul_f32 v[160:161], v[246:247], v[160:161] op_sel_hi:[0,1]
	v_cndmask_b32_e64 v118, v118, 4, s[76:77]
	v_pk_mul_f32 v[162:163], v[246:247], v[162:163] op_sel_hi:[0,1]
	v_mfma_f32_16x16x4_f32 v[216:219], v133, v23, v[216:219]
	v_sub_f32_e32 v121, v44, v114
	v_max_f32_dpp v115, v115, v115 row_ror:2 row_mask:0xf bank_mask:0xf
	v_cmp_eq_f32_e64 s[74:75], v44, v114
	v_exp_f32_e32 v137, v120
	global_store_dwordx4 v109, v[160:163], s[90:91] sc1
	v_cndmask_b32_e64 v118, v118, 3, s[72:73]
	v_pk_mul_f32 v[164:165], v[246:247], v[164:165] op_sel_hi:[0,1]
	v_sub_f32_e32 v120, v40, v114
	v_pk_mul_f32 v[166:167], v[246:247], v[166:167] op_sel_hi:[0,1]
	v_cmp_eq_f32_e64 s[76:77], v40, v114
	v_max_f32_dpp v115, v115, v115 row_ror:4 row_mask:0xf bank_mask:0xf
	v_exp_f32_e32 v136, v121
	global_store_dwordx4 v109, v[164:167], s[90:91] offset:256 sc1
	v_cndmask_b32_e64 v118, v118, 2, s[74:75]
	v_pk_mul_f32 v[168:169], v[246:247], v[168:169] op_sel_hi:[0,1]
	v_mfma_f32_16x16x4_f32 v[220:223], v133, v25, v[220:223]
	global_load_dwordx4 v[22:25], v104, s[88:89] offset:1024
	v_sub_f32_e32 v121, v36, v114
	v_pk_mul_f32 v[170:171], v[246:247], v[170:171] op_sel_hi:[0,1]
	v_cmp_eq_f32_e64 s[72:73], v36, v114
	global_store_dwordx4 v109, v[168:171], s[90:91] offset:512 sc1
	v_exp_f32_e32 v135, v120
	v_max_f32_dpp v115, v115, v115 row_ror:8 row_mask:0xf bank_mask:0xf
	v_cndmask_b32_e64 v118, v118, 1, s[76:77]
	v_pk_mul_f32 v[172:173], v[246:247], v[172:173] op_sel_hi:[0,1]
	v_exp_f32_e32 v134, v121
	v_pk_mul_f32 v[174:175], v[246:247], v[174:175] op_sel_hi:[0,1]
	v_cndmask_b32_e64 v118, v118, 0, s[72:73]
	global_store_dwordx4 v109, v[172:175], s[90:91] offset:768 sc1
	v_sub_f32_e32 v120, v97, v115
	v_cmp_eq_f32_e64 s[72:73], v97, v115
	s_waitcnt lgkmcnt(0)
	s_waitcnt vmcnt(28)
	v_mfma_f32_16x16x4_f32 v[224:227], v132, v26, 0
	v_sub_f32_e32 v121, v93, v115
	v_add_f32_e32 v250, v159, v250
	v_cmp_eq_f32_e64 s[74:75], v93, v115
	v_add_f32_e32 v251, v158, v251
	v_exp_f32_e32 v175, v120
	v_cndmask_b32_e64 v119, v155, 15, s[72:73]
	v_add_f32_e32 v252, v157, v252
	v_sub_f32_e32 v120, v89, v115
	v_add_f32_e32 v253, v156, v253
	v_cmp_eq_f32_e64 s[76:77], v89, v115
	ds_write2st64_b32 v113, v250, v251 offset1:12
	v_exp_f32_e32 v174, v121
	ds_write2st64_b32 v113, v252, v253 offset0:24 offset1:36
	v_cndmask_b32_e64 v119, v119, 14, s[74:75]
	v_mfma_f32_16x16x4_f32 v[228:231], v132, v28, 0
	v_sub_f32_e32 v121, v85, v115
	v_and_b32_e32 v122, 12, v118
	v_cmp_eq_f32_e64 s[72:73], v85, v115
	v_and_b32_e32 v124, 3, v118
	v_exp_f32_e32 v173, v120
	v_add_f32_e32 v128, v134, v135
	v_cndmask_b32_e64 v119, v119, 13, s[76:77]
	v_sub_f32_e32 v120, v81, v115
	v_add_f32_e32 v130, v136, v137
	v_cmp_eq_f32_e64 s[74:75], v81, v115
	v_lshl_or_b32 v122, v122, 4, v124
	v_exp_f32_e32 v172, v121
	v_add_f32_e32 v128, v128, v138
	v_cndmask_b32_e64 v119, v119, 12, s[72:73]
	v_add_f32_e32 v130, v130, v139
	v_mfma_f32_16x16x4_f32 v[224:227], v133, v27, v[224:227]
	v_sub_f32_e32 v121, v77, v115
	v_cmp_eq_f32_e64 s[76:77], v77, v115
	v_or_b32_e32 v122, v122, v102
	v_exp_f32_e32 v171, v120
	v_add_f32_e32 v128, v128, v140
	v_cndmask_b32_e64 v119, v119, 11, s[74:75]
	v_add_f32_e32 v130, v130, v141
	v_sub_f32_e32 v120, v73, v115
	v_cmp_eq_f32_e64 s[72:73], v73, v115
	v_max_u32_e32 v126, v122, v118
	v_exp_f32_e32 v170, v121
	v_add_f32_e32 v128, v128, v142
	v_cndmask_b32_e64 v119, v119, 10, s[76:77]
	v_add_f32_e32 v130, v130, v143
	v_mfma_f32_16x16x4_f32 v[228:231], v133, v29, v[228:231]
	global_load_dwordx4 v[26:29], v104, s[88:89] offset:2048
	v_sub_f32_e32 v121, v69, v115
	v_min_u32_dpp v126, v126, v126 row_ror:1 row_mask:0xf bank_mask:0xf
	v_cmp_eq_f32_e64 s[74:75], v69, v115
	v_exp_f32_e32 v169, v120
	v_add_f32_e32 v128, v128, v144
	v_cndmask_b32_e64 v119, v119, 9, s[72:73]
	v_add_f32_e32 v130, v130, v145
	v_sub_f32_e32 v120, v65, v115
	v_min_u32_dpp v126, v126, v126 row_ror:2 row_mask:0xf bank_mask:0xf
	v_cmp_eq_f32_e64 s[76:77], v65, v115
	v_add_f32_e32 v128, v128, v146
	v_exp_f32_e32 v168, v121
	v_cndmask_b32_e64 v119, v119, 8, s[74:75]
	v_add_f32_e32 v130, v130, v147
	s_waitcnt vmcnt(25)
	v_mfma_f32_16x16x4_f32 v[232:235], v132, v30, 0
	v_sub_f32_e32 v121, v61, v115
	v_min_u32_dpp v126, v126, v126 row_ror:4 row_mask:0xf bank_mask:0xf
	v_cmp_eq_f32_e64 s[72:73], v61, v115
	v_add_f32_e32 v128, v128, v148
	v_exp_f32_e32 v167, v120
	v_cndmask_b32_e64 v119, v119, 7, s[76:77]
	v_add_f32_e32 v130, v130, v149
	v_sub_f32_e32 v120, v57, v115
	v_min_u32_dpp v126, v126, v126 row_ror:8 row_mask:0xf bank_mask:0xf
	v_cmp_eq_f32_e64 s[74:75], v57, v115
	v_add_f32_e32 v128, v128, v130
	v_exp_f32_e32 v166, v121
	v_mad_u32_u24 v248, v126, 24, v107
	v_cndmask_b32_e64 v119, v119, 6, s[72:73]
	v_mfma_f32_16x16x4_f32 v[236:239], v132, v32, 0
	v_sub_f32_e32 v121, v53, v115
	v_add_f32_dpp v128, v128, v128 row_ror:1 row_mask:0xf bank_mask:0xf
	v_cmp_eq_f32_e64 s[76:77], v53, v115
	global_load_dword v242, v248, s[92:93]
	v_exp_f32_e32 v165, v120
	v_add_f32_dpp v128, v128, v128 row_ror:2 row_mask:0xf bank_mask:0xf
	v_cndmask_b32_e64 v119, v119, 5, s[74:75]
	v_sub_f32_e32 v120, v49, v115
	v_add_f32_dpp v128, v128, v128 row_ror:4 row_mask:0xf bank_mask:0xf
	v_cmp_eq_f32_e64 s[72:73], v49, v115
	s_nop 0
	v_add_f32_dpp v128, v128, v128 row_ror:8 row_mask:0xf bank_mask:0xf
	v_exp_f32_e32 v164, v121
	v_rcp_f32_e32 v244, v128
	v_cndmask_b32_e64 v119, v119, 4, s[76:77]
	v_pk_mul_f32 v[134:135], v[244:245], v[134:135] op_sel_hi:[0,1]
	v_mfma_f32_16x16x4_f32 v[232:235], v133, v31, v[232:235]
	v_sub_f32_e32 v121, v45, v115
	v_cmp_eq_f32_e64 s[74:75], v45, v115
	v_pk_mul_f32 v[136:137], v[244:245], v[136:137] op_sel_hi:[0,1]
	v_exp_f32_e32 v163, v120
	global_store_dwordx4 v110, v[134:137], s[90:91] sc1
	v_cndmask_b32_e64 v119, v119, 3, s[72:73]
	v_pk_mul_f32 v[138:139], v[244:245], v[138:139] op_sel_hi:[0,1]
	v_sub_f32_e32 v120, v41, v115
	v_cmp_eq_f32_e64 s[76:77], v41, v115
	v_pk_mul_f32 v[140:141], v[244:245], v[140:141] op_sel_hi:[0,1]
	v_exp_f32_e32 v162, v121
	global_store_dwordx4 v110, v[138:141], s[90:91] offset:256 sc1
	v_cndmask_b32_e64 v119, v119, 2, s[74:75]
	v_pk_mul_f32 v[142:143], v[244:245], v[142:143] op_sel_hi:[0,1]
	v_mfma_f32_16x16x4_f32 v[236:239], v133, v33, v[236:239]
	global_load_dwordx4 v[30:33], v104, s[88:89] offset:3072
	v_sub_f32_e32 v121, v37, v115
	v_pk_mul_f32 v[144:145], v[244:245], v[144:145] op_sel_hi:[0,1]
	v_cmp_eq_f32_e64 s[72:73], v37, v115
	v_exp_f32_e32 v161, v120
	global_store_dwordx4 v110, v[142:145], s[90:91] offset:512 sc1
	v_cndmask_b32_e64 v119, v119, 1, s[76:77]
	v_pk_mul_f32 v[146:147], v[244:245], v[146:147] op_sel_hi:[0,1]
	v_exp_f32_e32 v160, v121
	v_pk_mul_f32 v[148:149], v[244:245], v[148:149] op_sel_hi:[0,1]
	v_cndmask_b32_e64 v119, v119, 0, s[72:73]
	global_store_dwordx4 v110, v[146:149], s[90:91] offset:768 sc1
	v_and_b32_e32 v123, 12, v119
	v_max3_f32 v114, v176, v180, v184
	v_and_b32_e32 v125, 3, v119
	v_add_f32_e32 v129, v160, v161
	v_add_f32_e32 v131, v162, v163
	v_max3_f32 v116, v188, v192, v196
	v_lshl_or_b32 v123, v123, 4, v125
	v_add_f32_e32 v129, v129, v164
	v_add_f32_e32 v131, v131, v165
	v_or_b32_e32 v123, v123, v102
	v_max3_f32 v114, v114, v200, v204
	v_add_f32_e32 v129, v129, v166
	v_add_f32_e32 v131, v131, v167
	v_max_u32_e32 v127, v123, v119
	v_max3_f32 v116, v116, v208, v212
	v_add_f32_e32 v129, v129, v168
	v_add_f32_e32 v131, v131, v169
	v_min_u32_dpp v127, v127, v127 row_ror:1 row_mask:0xf bank_mask:0xf
	v_add_f32_e32 v129, v129, v170
	v_max3_f32 v114, v114, v216, v220
	v_add_f32_e32 v131, v131, v171
	v_min_u32_dpp v127, v127, v127 row_ror:2 row_mask:0xf bank_mask:0xf
	v_add_f32_e32 v129, v129, v172
	v_max3_f32 v116, v116, v224, v228
	v_add_f32_e32 v131, v131, v173
	v_min_u32_dpp v127, v127, v127 row_ror:4 row_mask:0xf bank_mask:0xf
	v_add_f32_e32 v129, v129, v174
	v_add_f32_e32 v131, v131, v175
	v_max3_f32 v114, v114, v232, v236
	v_min_u32_dpp v127, v127, v127 row_ror:8 row_mask:0xf bank_mask:0xf
	v_add_f32_e32 v129, v129, v131
	v_mad_u32_u24 v249, v127, 24, v107
	s_nop 0
	v_add_f32_dpp v129, v129, v129 row_ror:1 row_mask:0xf bank_mask:0xf
	v_max_f32_e32 v114, v114, v116
	global_load_dword v243, v249, s[92:93]
	v_add_f32_dpp v129, v129, v129 row_ror:2 row_mask:0xf bank_mask:0xf
	s_nop 1
	v_add_f32_dpp v129, v129, v129 row_ror:4 row_mask:0xf bank_mask:0xf
	v_max_f32_dpp v114, v114, v114 row_ror:1 row_mask:0xf bank_mask:0xf
	s_nop 0
	v_add_f32_dpp v129, v129, v129 row_ror:8 row_mask:0xf bank_mask:0xf
	v_rcp_f32_e32 v246, v129
	s_nop 0
	v_pk_mul_f32 v[160:161], v[246:247], v[160:161] op_sel_hi:[0,1]
	v_pk_mul_f32 v[162:163], v[246:247], v[162:163] op_sel_hi:[0,1]
	v_max_f32_dpp v114, v114, v114 row_ror:2 row_mask:0xf bank_mask:0xf
	global_store_dwordx4 v111, v[160:163], s[90:91] sc1
	v_pk_mul_f32 v[164:165], v[246:247], v[164:165] op_sel_hi:[0,1]
	v_pk_mul_f32 v[166:167], v[246:247], v[166:167] op_sel_hi:[0,1]
	v_max_f32_dpp v114, v114, v114 row_ror:4 row_mask:0xf bank_mask:0xf
	global_store_dwordx4 v111, v[164:167], s[90:91] offset:256 sc1
	v_pk_mul_f32 v[168:169], v[246:247], v[168:169] op_sel_hi:[0,1]
	v_pk_mul_f32 v[170:171], v[246:247], v[170:171] op_sel_hi:[0,1]
	global_store_dwordx4 v111, v[168:171], s[90:91] offset:512 sc1
	v_max_f32_dpp v114, v114, v114 row_ror:8 row_mask:0xf bank_mask:0xf
	v_pk_mul_f32 v[172:173], v[246:247], v[172:173] op_sel_hi:[0,1]
	v_pk_mul_f32 v[174:175], v[246:247], v[174:175] op_sel_hi:[0,1]
	global_store_dwordx4 v111, v[172:175], s[90:91] offset:768 sc1
	s_add_i32 s70, s70, 1
	s_waitcnt lgkmcnt(0)
	s_lshl_b32 s84, s70, 13
	s_add_u32 s90, s80, s84
	s_addc_u32 s91, s81, 0
	s_mul_i32 s84, s70, 0xc000
	s_add_u32 s92, s94, s84
	s_addc_u32 s93, s95, 0
	s_add_i32 s84, s70, 2
	s_and_b32 s84, s84, 15
	s_lshl_b32 s82, s84, 12
	s_lshl_b32 s84, s84, 16
	s_add_u32 s84, s84, 0x787000
	s_add_u32 s86, s40, s84
	s_addc_u32 s87, s41, 0
	s_add_u32 s88, s86, 0x1000
	s_addc_u32 s89, s87, 0
	s_add_i32 s84, s70, 15
	s_and_b32 s84, s84, 15
	s_mul_i32 s84, s84, 0xc0
	s_add_u32 s83, s84, 0x10000
	v_add_u32_e32 v112, s82, v105
	s_add_i32 s84, s70, 1
	s_and_b32 s84, s84, 15
	s_mul_i32 s84, s84, 0xc000
	s_add_u32 s58, s94, s84
	s_addc_u32 s59, s95, 0
	global_load_dword v98, v100, s[58:59]
	v_sub_f32_e32 v120, v236, v114
	v_cmp_eq_f32_e64 s[72:73], v236, v114
	s_waitcnt vmcnt(28)
	v_mfma_f32_16x16x4_f32 v[34:37], v254, v6, 0
	ds_read2st64_b32 v[132:133], v112 offset1:1
	v_sub_f32_e32 v121, v232, v114
	v_cmp_eq_f32_e64 s[74:75], v232, v114
	v_exp_f32_e32 v149, v120
	v_cndmask_b32_e64 v118, v155, 15, s[72:73]
	v_max3_f32 v115, v177, v181, v185
	v_sub_f32_e32 v120, v228, v114
	v_cmp_eq_f32_e64 s[76:77], v228, v114
	v_exp_f32_e32 v148, v121
	v_cndmask_b32_e64 v118, v118, 14, s[74:75]
	v_mfma_f32_16x16x4_f32 v[38:41], v254, v8, 0
	v_sub_f32_e32 v121, v224, v114
	v_max3_f32 v117, v189, v193, v197
	v_cmp_eq_f32_e64 s[72:73], v224, v114
	v_exp_f32_e32 v147, v120
	v_cndmask_b32_e64 v118, v118, 13, s[76:77]
	v_sub_f32_e32 v120, v220, v114
	v_cmp_eq_f32_e64 s[74:75], v220, v114
	v_max3_f32 v115, v115, v201, v205
	v_exp_f32_e32 v146, v121
	v_cndmask_b32_e64 v118, v118, 12, s[72:73]
	v_mfma_f32_16x16x4_f32 v[34:37], v255, v7, v[34:37]
	v_sub_f32_e32 v121, v216, v114
	v_cmp_eq_f32_e64 s[76:77], v216, v114
	v_exp_f32_e32 v145, v120
	v_cndmask_b32_e64 v118, v118, 11, s[74:75]
	v_max3_f32 v117, v117, v209, v213
	v_sub_f32_e32 v120, v212, v114
	v_cmp_eq_f32_e64 s[72:73], v212, v114
	v_exp_f32_e32 v144, v121
	v_cndmask_b32_e64 v118, v118, 10, s[76:77]
	v_mfma_f32_16x16x4_f32 v[38:41], v255, v9, v[38:41]
	global_load_dwordx4 v[6:9], v104, s[86:87]
	v_sub_f32_e32 v121, v208, v114
	v_max3_f32 v115, v115, v217, v221
	v_cmp_eq_f32_e64 s[74:75], v208, v114
	v_exp_f32_e32 v143, v120
	v_cndmask_b32_e64 v118, v118, 9, s[72:73]
	v_sub_f32_e32 v120, v204, v114
	v_cmp_eq_f32_e64 s[76:77], v204, v114
	v_max3_f32 v117, v117, v225, v229
	v_exp_f32_e32 v142, v121
	v_cndmask_b32_e64 v118, v118, 8, s[74:75]
	s_waitcnt vmcnt(28)
	v_mfma_f32_16x16x4_f32 v[42:45], v254, v2, 0
	v_sub_f32_e32 v121, v200, v114
	v_cmp_eq_f32_e64 s[72:73], v200, v114
	v_exp_f32_e32 v141, v120
	v_cndmask_b32_e64 v118, v118, 7, s[76:77]
	v_max3_f32 v115, v115, v233, v237
	v_sub_f32_e32 v120, v196, v114
	v_cmp_eq_f32_e64 s[74:75], v196, v114
	v_exp_f32_e32 v140, v121
	v_cndmask_b32_e64 v118, v118, 6, s[72:73]
	v_mfma_f32_16x16x4_f32 v[46:49], v254, v4, 0
	v_sub_f32_e32 v121, v192, v114
	v_max_f32_e32 v115, v115, v117
	v_cmp_eq_f32_e64 s[76:77], v192, v114
	v_exp_f32_e32 v139, v120
	v_cndmask_b32_e64 v118, v118, 5, s[74:75]
	v_sub_f32_e32 v120, v188, v114
	v_cmp_eq_f32_e64 s[72:73], v188, v114
	v_max_f32_dpp v115, v115, v115 row_ror:1 row_mask:0xf bank_mask:0xf
	v_exp_f32_e32 v138, v121
	v_cndmask_b32_e64 v118, v118, 4, s[76:77]
	v_mfma_f32_16x16x4_f32 v[42:45], v255, v3, v[42:45]
	v_sub_f32_e32 v121, v184, v114
	v_cmp_eq_f32_e64 s[74:75], v184, v114
	v_exp_f32_e32 v137, v120
	v_cndmask_b32_e64 v118, v118, 3, s[72:73]
	v_max_f32_dpp v115, v115, v115 row_ror:2 row_mask:0xf bank_mask:0xf
	v_sub_f32_e32 v120, v180, v114
	v_cmp_eq_f32_e64 s[76:77], v180, v114
	v_exp_f32_e32 v136, v121
	v_cndmask_b32_e64 v118, v118, 2, s[74:75]
	v_mfma_f32_16x16x4_f32 v[46:49], v255, v5, v[46:49]
	global_load_dwordx4 v[2:5], v104, s[86:87] offset:1024
	v_sub_f32_e32 v121, v176, v114
	v_max_f32_dpp v115, v115, v115 row_ror:4 row_mask:0xf bank_mask:0xf
	v_cmp_eq_f32_e64 s[72:73], v176, v114
	v_exp_f32_e32 v135, v120
	v_cndmask_b32_e64 v118, v118, 1, s[76:77]
	v_exp_f32_e32 v134, v121
	v_cndmask_b32_e64 v118, v118, 0, s[72:73]
	v_max_f32_dpp v115, v115, v115 row_ror:8 row_mask:0xf bank_mask:0xf
	v_sub_f32_e32 v120, v237, v115
	v_cmp_eq_f32_e64 s[72:73], v237, v115
	v_max3_f32 v114, v178, v182, v186
	s_waitcnt vmcnt(28)
	v_mfma_f32_16x16x4_f32 v[50:53], v254, v10, 0
	v_sub_f32_e32 v121, v233, v115
	v_and_b32_e32 v122, 12, v118
	v_cmp_eq_f32_e64 s[74:75], v233, v115
	v_and_b32_e32 v124, 3, v118
	v_exp_f32_e32 v175, v120
	v_add_f32_e32 v128, v134, v135
	v_cndmask_b32_e64 v119, v155, 15, s[72:73]
	v_add_f32_e32 v130, v136, v137
	v_sub_f32_e32 v120, v229, v115
	v_max3_f32 v116, v190, v194, v198
	v_cmp_eq_f32_e64 s[76:77], v229, v115
	v_exp_f32_e32 v174, v121
	v_lshl_or_b32 v122, v122, 4, v124
	v_cndmask_b32_e64 v119, v119, 14, s[74:75]
	v_add_f32_e32 v128, v128, v138
	v_mfma_f32_16x16x4_f32 v[54:57], v254, v12, 0
	v_sub_f32_e32 v121, v225, v115
	v_add_f32_e32 v130, v130, v139
	v_cmp_eq_f32_e64 s[72:73], v225, v115
	v_or_b32_e32 v122, v122, v102
	v_exp_f32_e32 v173, v120
	v_max3_f32 v114, v114, v202, v206
	v_cndmask_b32_e64 v119, v119, 13, s[76:77]
	v_add_f32_e32 v128, v128, v140
	v_sub_f32_e32 v120, v221, v115
	v_cmp_eq_f32_e64 s[74:75], v221, v115
	v_add_f32_e32 v130, v130, v141
	v_exp_f32_e32 v172, v121
	v_max_u32_e32 v126, v122, v118
	v_cndmask_b32_e64 v119, v119, 12, s[72:73]
	v_max3_f32 v116, v116, v210, v214
	v_mfma_f32_16x16x4_f32 v[50:53], v255, v11, v[50:53]
	v_sub_f32_e32 v121, v217, v115
	v_add_f32_e32 v128, v128, v142
	v_cmp_eq_f32_e64 s[76:77], v217, v115
	v_add_f32_e32 v130, v130, v143
	v_exp_f32_e32 v171, v120
	v_min_u32_dpp v126, v126, v126 row_ror:1 row_mask:0xf bank_mask:0xf
	v_cndmask_b32_e64 v119, v119, 11, s[74:75]
	v_sub_f32_e32 v120, v213, v115
	v_add_f32_e32 v128, v128, v144
	v_cmp_eq_f32_e64 s[72:73], v213, v115
	v_max3_f32 v114, v114, v218, v222
	v_exp_f32_e32 v170, v121
	v_add_f32_e32 v130, v130, v145
	v_cndmask_b32_e64 v119, v119, 10, s[76:77]
	v_min_u32_dpp v126, v126, v126 row_ror:2 row_mask:0xf bank_mask:0xf
	v_mfma_f32_16x16x4_f32 v[54:57], v255, v13, v[54:57]
	global_load_dwordx4 v[10:13], v104, s[86:87] offset:2048
	v_sub_f32_e32 v121, v209, v115
	v_add_f32_e32 v128, v128, v146
	v_cmp_eq_f32_e64 s[74:75], v209, v115
	v_max3_f32 v116, v116, v226, v230
	v_exp_f32_e32 v169, v120
	v_cndmask_b32_e64 v119, v119, 9, s[72:73]
	v_add_f32_e32 v130, v130, v147
	v_sub_f32_e32 v120, v205, v115
	v_min_u32_dpp v126, v126, v126 row_ror:4 row_mask:0xf bank_mask:0xf
	v_cmp_eq_f32_e64 s[76:77], v205, v115
	v_add_f32_e32 v128, v128, v148
	v_exp_f32_e32 v168, v121
	v_add_f32_e32 v130, v130, v149
	v_cndmask_b32_e64 v119, v119, 8, s[74:75]
	v_max3_f32 v114, v114, v234, v238
	s_waitcnt vmcnt(25)
	v_mfma_f32_16x16x4_f32 v[58:61], v254, v14, 0
	v_sub_f32_e32 v121, v201, v115
	v_min_u32_dpp v126, v126, v126 row_ror:8 row_mask:0xf bank_mask:0xf
	v_cmp_eq_f32_e64 s[72:73], v201, v115
	v_exp_f32_e32 v167, v120
	v_add_f32_e32 v128, v128, v130
	v_cndmask_b32_e64 v119, v119, 7, s[76:77]
	v_mad_u32_u24 v248, v126, 24, v107
	v_sub_f32_e32 v120, v197, v115
	v_add_f32_dpp v128, v128, v128 row_ror:1 row_mask:0xf bank_mask:0xf
	v_cmp_eq_f32_e64 s[74:75], v197, v115
	v_max_f32_e32 v114, v114, v116
	v_exp_f32_e32 v166, v121
	global_load_dword v159, v248, s[92:93]
	v_cndmask_b32_e64 v119, v119, 6, s[72:73]
	v_add_f32_dpp v128, v128, v128 row_ror:2 row_mask:0xf bank_mask:0xf
	v_mfma_f32_16x16x4_f32 v[62:65], v254, v16, 0
	v_sub_f32_e32 v121, v193, v115
	v_cmp_eq_f32_e64 s[76:77], v193, v115
	v_add_f32_dpp v128, v128, v128 row_ror:4 row_mask:0xf bank_mask:0xf
	v_exp_f32_e32 v165, v120
	v_max_f32_dpp v114, v114, v114 row_ror:1 row_mask:0xf bank_mask:0xf
	v_cndmask_b32_e64 v119, v119, 5, s[74:75]
	v_add_f32_dpp v128, v128, v128 row_ror:8 row_mask:0xf bank_mask:0xf
	v_sub_f32_e32 v120, v189, v115
	v_rcp_f32_e32 v244, v128
	v_cmp_eq_f32_e64 s[72:73], v189, v115
	v_pk_mul_f32 v[134:135], v[244:245], v[134:135] op_sel_hi:[0,1]
	v_exp_f32_e32 v164, v121
	v_pk_mul_f32 v[136:137], v[244:245], v[136:137] op_sel_hi:[0,1]
	v_cndmask_b32_e64 v119, v119, 4, s[76:77]
	v_mfma_f32_16x16x4_f32 v[58:61], v255, v15, v[58:61]
	v_sub_f32_e32 v121, v185, v115
	v_max_f32_dpp v114, v114, v114 row_ror:2 row_mask:0xf bank_mask:0xf
	v_cmp_eq_f32_e64 s[74:75], v185, v115
	global_store_dwordx4 v108, v[134:137], s[90:91] sc1
	v_exp_f32_e32 v163, v120
	v_pk_mul_f32 v[138:139], v[244:245], v[138:139] op_sel_hi:[0,1]
	v_cndmask_b32_e64 v119, v119, 3, s[72:73]
	v_pk_mul_f32 v[140:141], v[244:245], v[140:141] op_sel_hi:[0,1]
	v_sub_f32_e32 v120, v181, v115
	v_max_f32_dpp v114, v114, v114 row_ror:4 row_mask:0xf bank_mask:0xf
	v_cmp_eq_f32_e64 s[76:77], v181, v115
	global_store_dwordx4 v108, v[138:141], s[90:91] offset:256 sc1
	v_exp_f32_e32 v162, v121
	v_cndmask_b32_e64 v119, v119, 2, s[74:75]
	v_pk_mul_f32 v[142:143], v[244:245], v[142:143] op_sel_hi:[0,1]
	v_mfma_f32_16x16x4_f32 v[62:65], v255, v17, v[62:65]
	global_load_dwordx4 v[14:17], v104, s[86:87] offset:3072
	v_sub_f32_e32 v121, v177, v115
	v_pk_mul_f32 v[144:145], v[244:245], v[144:145] op_sel_hi:[0,1]
	v_cmp_eq_f32_e64 s[72:73], v177, v115
	global_store_dwordx4 v108, v[142:145], s[90:91] offset:512 sc1
	v_exp_f32_e32 v161, v120
	v_max_f32_dpp v114, v114, v114 row_ror:8 row_mask:0xf bank_mask:0xf
	v_cndmask_b32_e64 v119, v119, 1, s[76:77]
	v_pk_mul_f32 v[146:147], v[244:245], v[146:147] op_sel_hi:[0,1]
	v_exp_f32_e32 v160, v121
	v_pk_mul_f32 v[148:149], v[244:245], v[148:149] op_sel_hi:[0,1]
	v_cndmask_b32_e64 v119, v119, 0, s[72:73]
	global_store_dwordx4 v108, v[146:149], s[90:91] offset:768 sc1
	v_sub_f32_e32 v120, v238, v114
	v_cmp_eq_f32_e64 s[72:73], v238, v114
	s_waitcnt vmcnt(14)
	s_waitcnt vmcnt(28)
	v_mfma_f32_16x16x4_f32 v[66:69], v254, v18, 0
	v_sub_f32_e32 v121, v234, v114
	v_add_u32_e32 v113, s83, v106
	v_cmp_eq_f32_e64 s[74:75], v234, v114
	ds_read2st64_b32 v[250:251], v113 offset1:12
	v_exp_f32_e32 v149, v120
	ds_read2st64_b32 v[252:253], v113 offset0:24 offset1:36
	v_cndmask_b32_e64 v118, v155, 15, s[72:73]
	v_max3_f32 v115, v179, v183, v187
	v_sub_f32_e32 v120, v230, v114
	v_and_b32_e32 v123, 12, v119
	v_cmp_eq_f32_e64 s[76:77], v230, v114
	v_and_b32_e32 v125, 3, v119
	v_exp_f32_e32 v148, v121
	v_add_f32_e32 v129, v160, v161
	v_cndmask_b32_e64 v118, v118, 14, s[74:75]
	v_add_f32_e32 v131, v162, v163
	v_mfma_f32_16x16x4_f32 v[70:73], v254, v20, 0
	v_sub_f32_e32 v121, v226, v114
	v_max3_f32 v117, v191, v195, v199
	v_cmp_eq_f32_e64 s[72:73], v226, v114
	v_lshl_or_b32 v123, v123, 4, v125
	v_exp_f32_e32 v147, v120
	v_cndmask_b32_e64 v118, v118, 13, s[76:77]
	v_add_f32_e32 v129, v129, v164
	v_sub_f32_e32 v120, v222, v114
	v_add_f32_e32 v131, v131, v165
	v_cmp_eq_f32_e64 s[74:75], v222, v114
	v_or_b32_e32 v123, v123, v102
	v_exp_f32_e32 v146, v121
	v_max3_f32 v115, v115, v203, v207
	v_cndmask_b32_e64 v118, v118, 12, s[72:73]
	v_add_f32_e32 v129, v129, v166
	v_mfma_f32_16x16x4_f32 v[66:69], v255, v19, v[66:69]
	v_sub_f32_e32 v121, v218, v114
	v_add_f32_e32 v131, v131, v167
	v_cmp_eq_f32_e64 s[76:77], v218, v114
	v_max_u32_e32 v127, v123, v119
	v_exp_f32_e32 v145, v120
	v_max3_f32 v117, v117, v211, v215
	v_cndmask_b32_e64 v118, v118, 11, s[74:75]
	v_add_f32_e32 v129, v129, v168
	v_sub_f32_e32 v120, v214, v114
	v_add_f32_e32 v131, v131, v169
	v_cmp_eq_f32_e64 s[72:73], v214, v114
	v_min_u32_dpp v127, v127, v127 row_ror:1 row_mask:0xf bank_mask:0xf
	v_exp_f32_e32 v144, v121
	v_add_f32_e32 v129, v129, v170
	v_cndmask_b32_e64 v118, v118, 10, s[76:77]
	v_mfma_f32_16x16x4_f32 v[70:73], v255, v21, v[70:73]
	global_load_dwordx4 v[18:21], v104, s[88:89]
	v_sub_f32_e32 v121, v210, v114
	v_max3_f32 v115, v115, v219, v223
	v_cmp_eq_f32_e64 s[74:75], v210, v114
	v_add_f32_e32 v131, v131, v171
	v_exp_f32_e32 v143, v120
	v_min_u32_dpp v127, v127, v127 row_ror:2 row_mask:0xf bank_mask:0xf
	v_cndmask_b32_e64 v118, v118, 9, s[72:73]
	v_add_f32_e32 v129, v129, v172
	v_sub_f32_e32 v120, v206, v114
	v_max3_f32 v117, v117, v227, v231
	v_cmp_eq_f32_e64 s[76:77], v206, v114
	v_add_f32_e32 v131, v131, v173
	v_exp_f32_e32 v142, v121
	v_min_u32_dpp v127, v127, v127 row_ror:4 row_mask:0xf bank_mask:0xf
	v_cndmask_b32_e64 v118, v118, 8, s[74:75]
	v_add_f32_e32 v129, v129, v174
	s_waitcnt vmcnt(25)
	v_mfma_f32_16x16x4_f32 v[74:77], v254, v22, 0
	v_sub_f32_e32 v121, v202, v114
	v_add_f32_e32 v131, v131, v175
	v_cmp_eq_f32_e64 s[72:73], v202, v114
	v_max3_f32 v115, v115, v235, v239
	v_exp_f32_e32 v141, v120
	v_min_u32_dpp v127, v127, v127 row_ror:8 row_mask:0xf bank_mask:0xf
	v_cndmask_b32_e64 v118, v118, 7, s[76:77]
	v_add_f32_e32 v129, v129, v131
	v_sub_f32_e32 v120, v198, v114
	v_cmp_eq_f32_e64 s[74:75], v198, v114
	v_mad_u32_u24 v249, v127, 24, v107
	v_exp_f32_e32 v140, v121
	v_add_f32_dpp v129, v129, v129 row_ror:1 row_mask:0xf bank_mask:0xf
	v_cndmask_b32_e64 v118, v118, 6, s[72:73]
	v_max_f32_e32 v115, v115, v117
	v_mfma_f32_16x16x4_f32 v[78:81], v254, v24, 0
	v_sub_f32_e32 v121, v194, v114
	global_load_dword v158, v249, s[92:93]
	v_cmp_eq_f32_e64 s[76:77], v194, v114
	v_add_f32_dpp v129, v129, v129 row_ror:2 row_mask:0xf bank_mask:0xf
	v_exp_f32_e32 v139, v120
	s_nop 0
	v_add_f32_dpp v129, v129, v129 row_ror:4 row_mask:0xf bank_mask:0xf
	v_cndmask_b32_e64 v118, v118, 5, s[74:75]
	v_max_f32_dpp v115, v115, v115 row_ror:1 row_mask:0xf bank_mask:0xf
	v_sub_f32_e32 v120, v190, v114
	v_add_f32_dpp v129, v129, v129 row_ror:8 row_mask:0xf bank_mask:0xf
	v_cmp_eq_f32_e64 s[72:73], v190, v114
	v_rcp_f32_e32 v246, v129
	v_exp_f32_e32 v138, v121
	v_pk_mul_f32 v[160:161], v[246:247], v[160:161] op_sel_hi:[0,1]
	v_cndmask_b32_e64 v118, v118, 4, s[76:77]
	v_pk_mul_f32 v[162:163], v[246:247], v[162:163] op_sel_hi:[0,1]
	v_mfma_f32_16x16x4_f32 v[74:77], v255, v23, v[74:77]
	v_sub_f32_e32 v121, v186, v114
	v_max_f32_dpp v115, v115, v115 row_ror:2 row_mask:0xf bank_mask:0xf
	v_cmp_eq_f32_e64 s[74:75], v186, v114
	v_exp_f32_e32 v137, v120
	global_store_dwordx4 v109, v[160:163], s[90:91] sc1
	v_cndmask_b32_e64 v118, v118, 3, s[72:73]
	v_pk_mul_f32 v[164:165], v[246:247], v[164:165] op_sel_hi:[0,1]
	v_sub_f32_e32 v120, v182, v114
	v_pk_mul_f32 v[166:167], v[246:247], v[166:167] op_sel_hi:[0,1]
	v_cmp_eq_f32_e64 s[76:77], v182, v114
	v_max_f32_dpp v115, v115, v115 row_ror:4 row_mask:0xf bank_mask:0xf
	v_exp_f32_e32 v136, v121
	global_store_dwordx4 v109, v[164:167], s[90:91] offset:256 sc1
	v_cndmask_b32_e64 v118, v118, 2, s[74:75]
	v_pk_mul_f32 v[168:169], v[246:247], v[168:169] op_sel_hi:[0,1]
	v_mfma_f32_16x16x4_f32 v[78:81], v255, v25, v[78:81]
	global_load_dwordx4 v[22:25], v104, s[88:89] offset:1024
	v_sub_f32_e32 v121, v178, v114
	v_pk_mul_f32 v[170:171], v[246:247], v[170:171] op_sel_hi:[0,1]
	v_cmp_eq_f32_e64 s[72:73], v178, v114
	global_store_dwordx4 v109, v[168:171], s[90:91] offset:512 sc1
	v_exp_f32_e32 v135, v120
	v_max_f32_dpp v115, v115, v115 row_ror:8 row_mask:0xf bank_mask:0xf
	v_cndmask_b32_e64 v118, v118, 1, s[76:77]
	v_pk_mul_f32 v[172:173], v[246:247], v[172:173] op_sel_hi:[0,1]
	v_exp_f32_e32 v134, v121
	v_pk_mul_f32 v[174:175], v[246:247], v[174:175] op_sel_hi:[0,1]
	v_cndmask_b32_e64 v118, v118, 0, s[72:73]
	global_store_dwordx4 v109, v[172:175], s[90:91] offset:768 sc1
	v_sub_f32_e32 v120, v239, v115
	v_cmp_eq_f32_e64 s[72:73], v239, v115
	s_waitcnt lgkmcnt(0)
	s_waitcnt vmcnt(28)
	v_mfma_f32_16x16x4_f32 v[82:85], v254, v26, 0
	v_sub_f32_e32 v121, v235, v115
	v_add_f32_e32 v250, v240, v250
	v_cmp_eq_f32_e64 s[74:75], v235, v115
	v_add_f32_e32 v251, v241, v251
	v_exp_f32_e32 v175, v120
	v_cndmask_b32_e64 v119, v155, 15, s[72:73]
	v_add_f32_e32 v252, v242, v252
	v_sub_f32_e32 v120, v231, v115
	v_add_f32_e32 v253, v243, v253
	v_cmp_eq_f32_e64 s[76:77], v231, v115
	ds_write2st64_b32 v113, v250, v251 offset1:12
	v_exp_f32_e32 v174, v121
	ds_write2st64_b32 v113, v252, v253 offset0:24 offset1:36
	v_cndmask_b32_e64 v119, v119, 14, s[74:75]
	v_mfma_f32_16x16x4_f32 v[86:89], v254, v28, 0
	v_sub_f32_e32 v121, v227, v115
	v_and_b32_e32 v122, 12, v118
	v_cmp_eq_f32_e64 s[72:73], v227, v115
	v_and_b32_e32 v124, 3, v118
	v_exp_f32_e32 v173, v120
	v_add_f32_e32 v128, v134, v135
	v_cndmask_b32_e64 v119, v119, 13, s[76:77]
	v_sub_f32_e32 v120, v223, v115
	v_add_f32_e32 v130, v136, v137
	v_cmp_eq_f32_e64 s[74:75], v223, v115
	v_lshl_or_b32 v122, v122, 4, v124
	v_exp_f32_e32 v172, v121
	v_add_f32_e32 v128, v128, v138
	v_cndmask_b32_e64 v119, v119, 12, s[72:73]
	v_add_f32_e32 v130, v130, v139
	v_mfma_f32_16x16x4_f32 v[82:85], v255, v27, v[82:85]
	v_sub_f32_e32 v121, v219, v115
	v_cmp_eq_f32_e64 s[76:77], v219, v115
	v_or_b32_e32 v122, v122, v102
	v_exp_f32_e32 v171, v120
	v_add_f32_e32 v128, v128, v140
	v_cndmask_b32_e64 v119, v119, 11, s[74:75]
	v_add_f32_e32 v130, v130, v141
	v_sub_f32_e32 v120, v215, v115
	v_cmp_eq_f32_e64 s[72:73], v215, v115
	v_max_u32_e32 v126, v122, v118
	v_exp_f32_e32 v170, v121
	v_add_f32_e32 v128, v128, v142
	v_cndmask_b32_e64 v119, v119, 10, s[76:77]
	v_add_f32_e32 v130, v130, v143
	v_mfma_f32_16x16x4_f32 v[86:89], v255, v29, v[86:89]
	global_load_dwordx4 v[26:29], v104, s[88:89] offset:2048
	v_sub_f32_e32 v121, v211, v115
	v_min_u32_dpp v126, v126, v126 row_ror:1 row_mask:0xf bank_mask:0xf
	v_cmp_eq_f32_e64 s[74:75], v211, v115
	v_exp_f32_e32 v169, v120
	v_add_f32_e32 v128, v128, v144
	v_cndmask_b32_e64 v119, v119, 9, s[72:73]
	v_add_f32_e32 v130, v130, v145
	v_sub_f32_e32 v120, v207, v115
	v_min_u32_dpp v126, v126, v126 row_ror:2 row_mask:0xf bank_mask:0xf
	v_cmp_eq_f32_e64 s[76:77], v207, v115
	v_add_f32_e32 v128, v128, v146
	v_exp_f32_e32 v168, v121
	v_cndmask_b32_e64 v119, v119, 8, s[74:75]
	v_add_f32_e32 v130, v130, v147
	s_waitcnt vmcnt(25)
	v_mfma_f32_16x16x4_f32 v[90:93], v254, v30, 0
	v_sub_f32_e32 v121, v203, v115
	v_min_u32_dpp v126, v126, v126 row_ror:4 row_mask:0xf bank_mask:0xf
	v_cmp_eq_f32_e64 s[72:73], v203, v115
	v_add_f32_e32 v128, v128, v148
	v_exp_f32_e32 v167, v120
	v_cndmask_b32_e64 v119, v119, 7, s[76:77]
	v_add_f32_e32 v130, v130, v149
	v_sub_f32_e32 v120, v199, v115
	v_min_u32_dpp v126, v126, v126 row_ror:8 row_mask:0xf bank_mask:0xf
	v_cmp_eq_f32_e64 s[74:75], v199, v115
	v_add_f32_e32 v128, v128, v130
	v_exp_f32_e32 v166, v121
	v_mad_u32_u24 v248, v126, 24, v107
	v_cndmask_b32_e64 v119, v119, 6, s[72:73]
	v_mfma_f32_16x16x4_f32 v[94:97], v254, v32, 0
	v_sub_f32_e32 v121, v195, v115
	v_add_f32_dpp v128, v128, v128 row_ror:1 row_mask:0xf bank_mask:0xf
	v_cmp_eq_f32_e64 s[76:77], v195, v115
	global_load_dword v157, v248, s[92:93]
	v_exp_f32_e32 v165, v120
	v_add_f32_dpp v128, v128, v128 row_ror:2 row_mask:0xf bank_mask:0xf
	v_cndmask_b32_e64 v119, v119, 5, s[74:75]
	v_sub_f32_e32 v120, v191, v115
	v_add_f32_dpp v128, v128, v128 row_ror:4 row_mask:0xf bank_mask:0xf
	v_cmp_eq_f32_e64 s[72:73], v191, v115
	s_nop 0
	v_add_f32_dpp v128, v128, v128 row_ror:8 row_mask:0xf bank_mask:0xf
	v_exp_f32_e32 v164, v121
	v_rcp_f32_e32 v244, v128
	v_cndmask_b32_e64 v119, v119, 4, s[76:77]
	v_pk_mul_f32 v[134:135], v[244:245], v[134:135] op_sel_hi:[0,1]
	v_mfma_f32_16x16x4_f32 v[90:93], v255, v31, v[90:93]
	v_sub_f32_e32 v121, v187, v115
	v_cmp_eq_f32_e64 s[74:75], v187, v115
	v_pk_mul_f32 v[136:137], v[244:245], v[136:137] op_sel_hi:[0,1]
	v_exp_f32_e32 v163, v120
	global_store_dwordx4 v110, v[134:137], s[90:91] sc1
	v_cndmask_b32_e64 v119, v119, 3, s[72:73]
	v_pk_mul_f32 v[138:139], v[244:245], v[138:139] op_sel_hi:[0,1]
	v_sub_f32_e32 v120, v183, v115
	v_cmp_eq_f32_e64 s[76:77], v183, v115
	v_pk_mul_f32 v[140:141], v[244:245], v[140:141] op_sel_hi:[0,1]
	v_exp_f32_e32 v162, v121
	global_store_dwordx4 v110, v[138:141], s[90:91] offset:256 sc1
	v_cndmask_b32_e64 v119, v119, 2, s[74:75]
	v_pk_mul_f32 v[142:143], v[244:245], v[142:143] op_sel_hi:[0,1]
	v_mfma_f32_16x16x4_f32 v[94:97], v255, v33, v[94:97]
	global_load_dwordx4 v[30:33], v104, s[88:89] offset:3072
	v_sub_f32_e32 v121, v179, v115
	v_pk_mul_f32 v[144:145], v[244:245], v[144:145] op_sel_hi:[0,1]
	v_cmp_eq_f32_e64 s[72:73], v179, v115
	v_exp_f32_e32 v161, v120
	global_store_dwordx4 v110, v[142:145], s[90:91] offset:512 sc1
	v_cndmask_b32_e64 v119, v119, 1, s[76:77]
	v_pk_mul_f32 v[146:147], v[244:245], v[146:147] op_sel_hi:[0,1]
	v_exp_f32_e32 v160, v121
	v_pk_mul_f32 v[148:149], v[244:245], v[148:149] op_sel_hi:[0,1]
	v_cndmask_b32_e64 v119, v119, 0, s[72:73]
	global_store_dwordx4 v110, v[146:149], s[90:91] offset:768 sc1
	v_and_b32_e32 v123, 12, v119
	v_max3_f32 v114, v34, v38, v42
	v_and_b32_e32 v125, 3, v119
	v_add_f32_e32 v129, v160, v161
	v_add_f32_e32 v131, v162, v163
	v_max3_f32 v116, v46, v50, v54
	v_lshl_or_b32 v123, v123, 4, v125
	v_add_f32_e32 v129, v129, v164
	v_add_f32_e32 v131, v131, v165
	v_or_b32_e32 v123, v123, v102
	v_max3_f32 v114, v114, v58, v62
	v_add_f32_e32 v129, v129, v166
	v_add_f32_e32 v131, v131, v167
	v_max_u32_e32 v127, v123, v119
	v_max3_f32 v116, v116, v66, v70
	v_add_f32_e32 v129, v129, v168
	v_add_f32_e32 v131, v131, v169
	v_min_u32_dpp v127, v127, v127 row_ror:1 row_mask:0xf bank_mask:0xf
	v_add_f32_e32 v129, v129, v170
	v_max3_f32 v114, v114, v74, v78
	v_add_f32_e32 v131, v131, v171
	v_min_u32_dpp v127, v127, v127 row_ror:2 row_mask:0xf bank_mask:0xf
	v_add_f32_e32 v129, v129, v172
	v_max3_f32 v116, v116, v82, v86
	v_add_f32_e32 v131, v131, v173
	v_min_u32_dpp v127, v127, v127 row_ror:4 row_mask:0xf bank_mask:0xf
	v_add_f32_e32 v129, v129, v174
	v_add_f32_e32 v131, v131, v175
	v_max3_f32 v114, v114, v90, v94
	v_min_u32_dpp v127, v127, v127 row_ror:8 row_mask:0xf bank_mask:0xf
	v_add_f32_e32 v129, v129, v131
	v_mad_u32_u24 v249, v127, 24, v107
	s_nop 0
	v_add_f32_dpp v129, v129, v129 row_ror:1 row_mask:0xf bank_mask:0xf
	v_max_f32_e32 v114, v114, v116
	global_load_dword v156, v249, s[92:93]
	v_add_f32_dpp v129, v129, v129 row_ror:2 row_mask:0xf bank_mask:0xf
	s_nop 1
	v_add_f32_dpp v129, v129, v129 row_ror:4 row_mask:0xf bank_mask:0xf
	v_max_f32_dpp v114, v114, v114 row_ror:1 row_mask:0xf bank_mask:0xf
	s_nop 0
	v_add_f32_dpp v129, v129, v129 row_ror:8 row_mask:0xf bank_mask:0xf
	v_rcp_f32_e32 v246, v129
	s_nop 0
	v_pk_mul_f32 v[160:161], v[246:247], v[160:161] op_sel_hi:[0,1]
	v_pk_mul_f32 v[162:163], v[246:247], v[162:163] op_sel_hi:[0,1]
	v_max_f32_dpp v114, v114, v114 row_ror:2 row_mask:0xf bank_mask:0xf
	global_store_dwordx4 v111, v[160:163], s[90:91] sc1
	v_pk_mul_f32 v[164:165], v[246:247], v[164:165] op_sel_hi:[0,1]
	v_pk_mul_f32 v[166:167], v[246:247], v[166:167] op_sel_hi:[0,1]
	v_max_f32_dpp v114, v114, v114 row_ror:4 row_mask:0xf bank_mask:0xf
	global_store_dwordx4 v111, v[164:167], s[90:91] offset:256 sc1
	v_pk_mul_f32 v[168:169], v[246:247], v[168:169] op_sel_hi:[0,1]
	v_pk_mul_f32 v[170:171], v[246:247], v[170:171] op_sel_hi:[0,1]
	global_store_dwordx4 v111, v[168:171], s[90:91] offset:512 sc1
	v_max_f32_dpp v114, v114, v114 row_ror:8 row_mask:0xf bank_mask:0xf
	v_pk_mul_f32 v[172:173], v[246:247], v[172:173] op_sel_hi:[0,1]
	v_pk_mul_f32 v[174:175], v[246:247], v[174:175] op_sel_hi:[0,1]
	global_store_dwordx4 v111, v[172:175], s[90:91] offset:768 sc1
	s_add_i32 s70, s70, 1
	s_cmp_lt_u32 s70, 16
	s_cbranch_scc1 .Lk3m_loop
